# speedup vs baseline: 1.0066x; 1.0066x over previous
.Lsub:
	s_setprio 2
	ds_read_b64 v[36:37], v2
	v_cmp_gt_u32_e32 vcc, v3, v8
	v_add_u32_e32 v2, 64, v2
	v_add_u32_e32 v8, 16, v8
	v_mov_b32_e32 v33, 0x3c00
	s_waitcnt lgkmcnt(0)
	v_perm_b32 v32, v37, v36, v57
	v_cndmask_b32_e32 v33, 0, v33, vcc
	s_nop 0
	v_cndmask_b32_e32 v32, 0, v32, vcc
	s_nop 1
	v_mfma_f32_32x32x16_f16 v[96:111], v[32:35], v[64:67], 0
	v_mfma_f32_32x32x16_f16 v[112:127], v[32:35], v[68:71], 0
	s_nop 10
	s_sub_u32 s45, s43, s44
	s_min_u32 s46, s45, 16
	s_cmp_eq_u32 s46, 2
	s_cbranch_scc1 .Ln2
	s_cmp_eq_u32 s46, 3
	s_cbranch_scc1 .Ln3
	s_cmp_eq_u32 s46, 4
	s_cbranch_scc1 .Ln4
	s_cmp_eq_u32 s46, 5
	s_cbranch_scc1 .Ln5
	s_cmp_eq_u32 s46, 6
	s_cbranch_scc1 .Ln6
	s_cmp_eq_u32 s46, 7
	s_cbranch_scc1 .Ln7
	s_cmp_eq_u32 s46, 8
	s_cbranch_scc1 .Ln8
	s_cmp_eq_u32 s46, 9
	s_cbranch_scc1 .Ln9
	s_cmp_eq_u32 s46, 10
	s_cbranch_scc1 .Ln10
	s_cmp_eq_u32 s46, 11
	s_cbranch_scc1 .Ln11
	s_cmp_eq_u32 s46, 12
	s_cbranch_scc1 .Ln12
	s_cmp_eq_u32 s46, 13
	s_cbranch_scc1 .Ln13
	s_cmp_eq_u32 s46, 14
	s_cbranch_scc1 .Ln14
	s_cmp_eq_u32 s46, 15
	s_cbranch_scc1 .Ln15
	s_cmp_eq_u32 s46, 16
	s_cbranch_scc1 .Ln16
